# speedup vs baseline: 1.0215x; 1.0215x over previous
.LBB1_48:
	s_or_b64 exec, exec, s[0:1]
	s_add_i32 s27, s30, 1
	s_lshl_b32 s0, s27, 18
	s_add_u32 s4, s44, s0
	s_addc_u32 s5, s45, 0
	s_lshl_b32 s0, s30, 2
	v_readlane_b32 s1, v240, 2
	s_add_i32 s0, s0, s1
	s_lshl_b32 s8, s0, 2
	s_mov_b32 s9, s31
	s_lshl_b64 s[0:1], s[8:9], 8
	s_add_u32 s0, s62, s0
	s_addc_u32 s1, s63, s1
	v_cmp_gt_i32_e32 vcc, 64, v179
	s_waitcnt lgkmcnt(0)
	s_barrier
	s_and_saveexec_b64 s[20:21], vcc
	s_cbranch_execz .LBB1_52
	v_ashrrev_i32_e32 v98, 5, v179
	v_bfe_u32 v101, v179, 1, 4
	v_and_b32_e32 v103, 1, v179
	s_add_i32 s9, 0, 0x18000
	v_lshl_add_u32 v104, v98, 9, s9
	v_lshlrev_b32_e32 v105, 5, v101
	v_lshlrev_b32_e32 v106, 4, v103
	v_add3_u32 v106, v104, v105, v106
	v_lshlrev_b32_e32 v104, 13, v98
	v_ashrrev_i32_e32 v105, 31, v104
	v_or_b32_e32 v103, s74, v103
	v_lshl_add_u64 v[104:105], v[104:105], 4, s[4:5]
	v_lshl_add_u64 v[104:105], s[28:29], 4, v[104:105]
	v_lshlrev_b32_e32 v98, 8, v103
	v_lshl_add_u64 v[104:105], v[104:105], 0, v[98:99]
	v_lshlrev_b32_e32 v98, 4, v101
	v_lshl_add_u64 v[110:111], v[104:105], 0, v[98:99]
	ds_read_b128 v[104:107], v106
	s_waitcnt lgkmcnt(0)
	global_store_dwordx4 v[110:111], v[104:107], off sc0 sc1
	s_nop 0
	v_cmp_eq_u32_e32 vcc, 0, v179
	s_and_b64 exec, exec, vcc
	s_cbranch_execz .LBB1_52
	s_mov_b64 s[96:97], exec
	v_mbcnt_lo_u32_b32 v98, s96, 0
	v_mbcnt_hi_u32_b32 v98, s97, v98
	v_cmp_eq_u32_e32 vcc, 0, v98
	s_and_b64 vcc, exec, vcc
	s_mov_b64 exec, vcc
	s_cbranch_execz .LBB1_52
	v_readlane_b32 s9, v240, 14
	s_lshl_b32 s9, s9, 2
	s_bcnt1_i32_b64 s91, s[96:97]
	v_mov_b32_e32 v98, s9
	v_mov_b32_e32 v101, s91
	global_atomic_add v98, v101, s[0:1]

.LBB1_69:
	s_or_b64 exec, exec, s[4:5]
	s_add_i32 s0, s8, 0x200
	s_mov_b32 s1, s31
	s_lshl_b32 s9, s27, 17
	s_lshl_b64 s[0:1], s[0:1], 8
	s_add_u32 s4, s62, s0
	s_addc_u32 s5, s63, s1
	s_lshl_b32 s9, s9, 1
	s_add_u32 s0, s46, s9
	s_addc_u32 s1, s47, 0
	v_cmp_gt_i32_e32 vcc, 64, v179
	s_waitcnt lgkmcnt(0)
	s_barrier
	s_and_saveexec_b64 s[18:19], vcc
	s_cbranch_execz .LBB1_73
	v_ashrrev_i32_e32 v98, 5, v179
	v_bfe_u32 v103, v179, 1, 4
	v_and_b32_e32 v100, 1, v179
	s_add_i32 s20, 0, 0x18000
	v_lshl_add_u32 v101, v98, 9, s20
	v_lshlrev_b32_e32 v104, 5, v103
	v_lshlrev_b32_e32 v105, 4, v100
	v_add3_u32 v104, v101, v104, v105
	v_or_b32_e32 v105, s74, v100
	v_lshlrev_b32_e32 v100, 13, v98
	v_ashrrev_i32_e32 v101, 31, v100
	v_lshl_add_u64 v[100:101], v[100:101], 4, s[0:1]
	v_lshl_add_u64 v[100:101], s[28:29], 4, v[100:101]
	v_lshlrev_b32_e32 v98, 8, v105
	v_lshl_add_u64 v[100:101], v[100:101], 0, v[98:99]
	v_lshlrev_b32_e32 v98, 4, v103
	v_lshl_add_u64 v[100:101], v[100:101], 0, v[98:99]
	ds_read_b128 v[104:107], v104
	s_waitcnt lgkmcnt(0)
	global_store_dwordx4 v[100:101], v[104:107], off sc0 sc1
	s_nop 0
	v_cmp_eq_u32_e32 vcc, 0, v179
	s_and_b64 exec, exec, vcc
	s_cbranch_execz .LBB1_73
	s_mov_b64 s[20:21], exec
	v_mbcnt_lo_u32_b32 v98, s20, 0
	v_mbcnt_hi_u32_b32 v98, s21, v98
	v_cmp_eq_u32_e32 vcc, 0, v98
	s_and_b64 s[96:97], exec, vcc
	s_mov_b64 exec, s[96:97]
	s_cbranch_execz .LBB1_73
	v_readlane_b32 s91, v240, 14
	s_lshl_b32 s91, s91, 2
	s_bcnt1_i32_b64 s20, s[20:21]
	v_mov_b32_e32 v98, s91
	v_mov_b32_e32 v100, s20
	global_atomic_add v98, v100, s[4:5]

.LBB1_117:
	s_nop 0
	s_barrier
	s_mov_b64 s[0:1], exec
	v_readlane_b32 s4, v240, 4
	v_readlane_b32 s5, v240, 5
	s_and_b64 s[4:5], s[0:1], s[4:5]
	s_mov_b64 exec, s[4:5]
	s_cbranch_execz .LBB1_120
	s_mov_b64 s[4:5], exec
	v_mbcnt_lo_u32_b32 v98, s4, 0
	v_mbcnt_hi_u32_b32 v98, s5, v98
	v_cmp_eq_u32_e32 vcc, 0, v98
	s_and_b64 s[18:19], exec, vcc
	s_mov_b64 exec, s[18:19]
	s_cbranch_execz .LBB1_120
	s_add_i32 s30, s8, 0x600
	s_lshl_b64 s[8:9], s[30:31], 8
	v_readlane_b32 s18, v240, 27
	s_add_u32 s8, s18, s8
	v_readlane_b32 s18, v240, 28
	s_addc_u32 s9, s18, s9
	s_bcnt1_i32_b64 s4, s[4:5]
	v_mov_b32_e32 v98, s4
	global_atomic_add v99, v98, s[8:9]

.LBB2_34:
	v_mov_b32_e32 v1, 0x1e000
	v_sub_f32_e32 v20, v13, v2
	v_sub_f32_e32 v18, v9, v2
	v_sub_f32_e32 v21, v11, v2
	v_sub_f32_e32 v19, v7, v2
	v_lshl_or_b32 v0, v0, 5, v1
	v_sub_f32_e32 v6, v17, v2
	v_sub_f32_e32 v4, v10, v2
	v_sub_f32_e32 v7, v12, v2
	v_sub_f32_e32 v5, v8, v2
	global_store_dwordx4 v0, v[18:21], s[0:1] nt
	global_store_dwordx4 v0, v[4:7], s[0:1] offset:16 nt
	s_endpgm
	s_nop 0
	s_nop 0
	s_nop 0
	s_nop 0
	s_nop 0
	s_nop 0
	s_nop 0
	s_nop 0
	s_nop 0
	s_nop 0
	s_nop 0
	s_nop 0
	s_nop 0
	s_nop 0
	s_nop 0
	s_nop 0
	s_nop 0
	s_nop 0
	s_nop 0
	s_nop 0
	s_nop 0
	s_nop 0
	s_nop 0
	s_nop 0
	s_nop 0
	s_nop 0
	s_nop 0
	s_nop 0
	s_nop 0
	s_nop 0
	s_nop 0
	s_nop 0
	s_nop 0
	s_nop 0
	s_nop 0
	s_nop 0
	s_nop 0
	s_nop 0
	s_nop 0
	s_nop 0
	s_nop 0
	s_nop 0
	s_nop 0
	s_nop 0
	s_nop 0
	s_nop 0
	s_nop 0
	s_endpgm

.LBB3_10:
	s_or_b64 exec, exec, s[0:1]
	v_lshlrev_b32_e32 v0, 5, v1
	v_or3_b32 v0, v0, s10, v158
	v_ashrrev_i32_e32 v1, 31, v0
	v_lshlrev_b64 v[0:1], 2, v[0:1]
	v_lshl_add_u64 v[130:131], s[14:15], 0, v[0:1]
	global_load_dword v151, v[130:131], off
	global_load_dword v160, v[130:131], off offset:64
	global_load_dword v161, v[130:131], off
	v_and_b32_e32 v132, 12, v154
	v_or3_b32 v150, v132, v144, s12
	v_or_b32_e32 v134, 1, v150
	v_or_b32_e32 v136, 2, v150
	v_or_b32_e32 v138, 3, v150
	v_or_b32_e32 v142, 17, v150
	v_or_b32_e32 v143, 18, v150
	v_or_b32_e32 v144, 19, v150
	v_or_b32_e32 v145, 32, v150
	v_mad_i64_i32 v[132:133], s[0:1], v150, s9, 0
	v_mad_i64_i32 v[134:135], s[0:1], v134, s9, 0
	v_mad_i64_i32 v[136:137], s[0:1], v136, s9, 0
	v_mad_i64_i32 v[138:139], s[0:1], v138, s9, 0
	v_mad_i64_i32 v[152:153], s[0:1], v142, s9, 0
	v_mad_i64_i32 v[154:155], s[0:1], v143, s9, 0
	v_mad_i64_i32 v[156:157], s[0:1], v144, s9, 0
	v_mad_i64_i32 v[158:159], s[0:1], v145, s9, 0
	v_lshl_add_u64 v[0:1], s[2:3], 0, v[0:1]
	v_lshl_add_u64 v[148:149], v[132:133], 2, v[0:1]
	v_lshl_add_u64 v[146:147], v[134:135], 2, v[0:1]
	v_lshl_add_u64 v[144:145], v[136:137], 2, v[0:1]
	v_lshl_add_u64 v[142:143], v[138:139], 2, v[0:1]
	v_lshl_add_u64 v[138:139], v[152:153], 2, v[0:1]
	v_lshl_add_u64 v[136:137], v[154:155], 2, v[0:1]
	v_lshl_add_u64 v[134:135], v[156:157], 2, v[0:1]
	v_lshl_add_u64 v[132:133], v[158:159], 2, v[0:1]
	global_load_dword v152, v[130:131], off offset:512
	global_load_dword v153, v[130:131], off offset:576
	global_load_dword v154, v[130:131], off offset:64
	global_load_dword v155, v[130:131], off
	global_load_dword v156, v[130:131], off offset:64
	global_load_dword v157, v[130:131], off offset:64
	global_load_dword v158, v[130:131], off
	v_or_b32_e32 v140, 16, v150
	v_mad_i64_i32 v[140:141], s[0:1], v140, s9, 0
	v_lshl_add_u64 v[140:141], v[140:141], 2, v[0:1]
	s_waitcnt vmcnt(0)
	v_add_f32_e32 v126, v151, v126
	v_add_f32_e32 v110, v151, v110
	v_add_f32_e32 v127, v151, v127
	v_add_f32_e32 v128, v151, v128
	v_add_f32_e32 v129, v151, v129
	v_add_f32_e32 v122, v160, v122
	v_add_f32_e32 v123, v160, v123
	v_add_f32_e32 v124, v160, v124
	v_add_f32_e32 v125, v160, v125
	v_add_f32_e32 v118, v151, v118
	v_add_f32_e32 v119, v151, v119
	v_add_f32_e32 v120, v151, v120
	v_add_f32_e32 v121, v151, v121
	v_add_f32_e32 v114, v160, v114
	v_add_f32_e32 v115, v160, v115
	v_add_f32_e32 v116, v160, v116
	v_add_f32_e32 v117, v160, v117
	global_store_dword v[148:149], v126, off
	global_store_dword v[146:147], v127, off
	global_store_dword v[144:145], v128, off
	global_store_dword v[142:143], v129, off
	global_store_dword v[148:149], v122, off offset:64
	global_store_dword v[146:147], v123, off offset:64
	global_store_dword v[144:145], v124, off offset:64
	global_store_dword v[142:143], v125, off offset:64
	global_store_dword v[140:141], v118, off
	global_store_dword v[138:139], v119, off
	global_store_dword v[136:137], v120, off
	global_store_dword v[134:135], v121, off
	global_store_dword v[140:141], v114, off offset:64
	global_store_dword v[138:139], v115, off offset:64
	global_store_dword v[136:137], v116, off offset:64
	global_store_dword v[134:135], v117, off offset:64
	global_store_dword v[132:133], v110, off
	v_or_b32_e32 v110, 33, v150
	v_add_f32_e32 v114, v151, v111
	v_mad_i64_i32 v[110:111], s[0:1], v110, s9, 0
	v_lshl_add_u64 v[110:111], v[110:111], 2, v[0:1]
	global_store_dword v[110:111], v114, off
	v_or_b32_e32 v114, 34, v150
	v_mad_i64_i32 v[114:115], s[0:1], v114, s9, 0
	v_add_f32_e32 v112, v151, v112
	v_lshl_add_u64 v[114:115], v[114:115], 2, v[0:1]
	global_store_dword v[114:115], v112, off
	v_or_b32_e32 v112, 35, v150
	v_add_f32_e32 v116, v151, v113
	v_mad_i64_i32 v[112:113], s[0:1], v112, s9, 0
	v_lshl_add_u64 v[112:113], v[112:113], 2, v[0:1]
	v_add_f32_e32 v106, v160, v106
	global_store_dword v[112:113], v116, off
	global_store_dword v[132:133], v106, off offset:64
	v_add_f32_e32 v106, v160, v107
	global_store_dword v[110:111], v106, off offset:64
	v_add_f32_e32 v106, v160, v108
	global_store_dword v[114:115], v106, off offset:64
	v_add_f32_e32 v106, v160, v109
	global_store_dword v[112:113], v106, off offset:64
	v_or_b32_e32 v106, 48, v150
	v_mad_i64_i32 v[106:107], s[0:1], v106, s9, 0
	v_add_f32_e32 v102, v161, v102
	v_lshl_add_u64 v[106:107], v[106:107], 2, v[0:1]
	global_store_dword v[106:107], v102, off
	v_or_b32_e32 v102, 49, v150
	v_add_f32_e32 v108, v161, v103
	v_mad_i64_i32 v[102:103], s[0:1], v102, s9, 0
	v_lshl_add_u64 v[102:103], v[102:103], 2, v[0:1]
	global_store_dword v[102:103], v108, off
	v_or_b32_e32 v108, 50, v150
	v_mad_i64_i32 v[108:109], s[0:1], v108, s9, 0
	v_add_f32_e32 v104, v161, v104
	v_lshl_add_u64 v[108:109], v[108:109], 2, v[0:1]
	global_store_dword v[108:109], v104, off
	v_or_b32_e32 v104, 51, v150
	v_add_f32_e32 v116, v161, v105
	v_mad_i64_i32 v[104:105], s[0:1], v104, s9, 0
	v_lshl_add_u64 v[104:105], v[104:105], 2, v[0:1]
	v_add_f32_e32 v98, v154, v98
	global_store_dword v[104:105], v116, off
	global_store_dword v[106:107], v98, off offset:64
	v_add_f32_e32 v98, v154, v99
	global_store_dword v[102:103], v98, off offset:64
	v_add_f32_e32 v98, v154, v100
	global_store_dword v[108:109], v98, off offset:64
	v_add_f32_e32 v98, v154, v101
	global_store_dword v[104:105], v98, off offset:64
	v_add_f32_e32 v94, v152, v94
	global_load_dword v98, v[130:131], off offset:576
	global_load_dword v99, v[130:131], off offset:512
	v_add_f32_e32 v90, v153, v90
	global_store_dword v[148:149], v94, off offset:512
	v_add_f32_e32 v94, v152, v95
	global_store_dword v[146:147], v94, off offset:512
	v_add_f32_e32 v94, v152, v96
	global_store_dword v[144:145], v94, off offset:512
	v_add_f32_e32 v94, v152, v97
	global_store_dword v[142:143], v94, off offset:512
	global_store_dword v[148:149], v90, off offset:576
	v_add_f32_e32 v90, v153, v91
	global_store_dword v[146:147], v90, off offset:576
	v_add_f32_e32 v90, v153, v92
	global_store_dword v[144:145], v90, off offset:576
	v_add_f32_e32 v90, v153, v93
	v_add_f32_e32 v86, v152, v86
	global_store_dword v[142:143], v90, off offset:576
	global_store_dword v[140:141], v86, off offset:512
	v_add_f32_e32 v86, v152, v87
	global_store_dword v[138:139], v86, off offset:512
	v_add_f32_e32 v86, v152, v88
	global_store_dword v[136:137], v86, off offset:512
	v_add_f32_e32 v86, v152, v89
	v_add_f32_e32 v82, v153, v82
	global_store_dword v[134:135], v86, off offset:512
	global_store_dword v[140:141], v82, off offset:576
	v_add_f32_e32 v82, v153, v83
	global_store_dword v[138:139], v82, off offset:576
	v_add_f32_e32 v82, v153, v84
	global_store_dword v[136:137], v82, off offset:576
	v_add_f32_e32 v82, v153, v85
	v_add_f32_e32 v78, v152, v78
	global_store_dword v[134:135], v82, off offset:576
	global_store_dword v[132:133], v78, off offset:512
	v_add_f32_e32 v78, v152, v79
	global_store_dword v[110:111], v78, off offset:512
	v_add_f32_e32 v78, v152, v80
	global_store_dword v[114:115], v78, off offset:512
	v_add_f32_e32 v78, v152, v81
	v_add_f32_e32 v74, v153, v74
	global_store_dword v[112:113], v78, off offset:512
	global_store_dword v[132:133], v74, off offset:576
	v_add_f32_e32 v74, v153, v75
	global_store_dword v[110:111], v74, off offset:576
	v_add_f32_e32 v74, v153, v76
	global_store_dword v[114:115], v74, off offset:576
	v_add_f32_e32 v74, v153, v77
	v_add_f32_e32 v70, v152, v70
	global_store_dword v[112:113], v74, off offset:576
	global_store_dword v[106:107], v70, off offset:512
	v_add_f32_e32 v70, v152, v71
	global_store_dword v[102:103], v70, off offset:512
	v_add_f32_e32 v70, v152, v72
	global_store_dword v[108:109], v70, off offset:512
	v_add_f32_e32 v70, v152, v73
	v_add_f32_e32 v66, v153, v66
	global_store_dword v[104:105], v70, off offset:512
	global_store_dword v[106:107], v66, off offset:576
	v_add_f32_e32 v66, v153, v67
	global_store_dword v[102:103], v66, off offset:576
	v_add_f32_e32 v66, v153, v68
	global_store_dword v[108:109], v66, off offset:576
	v_add_f32_e32 v66, v153, v69
	global_store_dword v[104:105], v66, off offset:576
	v_add_u32_e32 v66, 0x80, v150
	v_mad_i64_i32 v[66:67], s[0:1], v66, s9, 0
	v_add_f32_e32 v62, v155, v62
	v_lshl_add_u64 v[66:67], v[66:67], 2, v[0:1]
	global_store_dword v[66:67], v62, off
	v_add_u32_e32 v62, 0x81, v150
	v_add_f32_e32 v68, v155, v63
	v_mad_i64_i32 v[62:63], s[0:1], v62, s9, 0
	v_lshl_add_u64 v[62:63], v[62:63], 2, v[0:1]
	global_store_dword v[62:63], v68, off
	v_add_u32_e32 v68, 0x82, v150
	v_mad_i64_i32 v[68:69], s[0:1], v68, s9, 0
	v_add_f32_e32 v64, v155, v64
	v_lshl_add_u64 v[68:69], v[68:69], 2, v[0:1]
	global_store_dword v[68:69], v64, off
	v_add_u32_e32 v64, 0x83, v150
	v_add_f32_e32 v70, v155, v65
	v_mad_i64_i32 v[64:65], s[0:1], v64, s9, 0
	v_lshl_add_u64 v[64:65], v[64:65], 2, v[0:1]
	v_add_f32_e32 v58, v156, v58
	global_store_dword v[64:65], v70, off
	global_store_dword v[66:67], v58, off offset:64
	v_add_f32_e32 v58, v156, v59
	global_store_dword v[62:63], v58, off offset:64
	v_add_f32_e32 v58, v156, v60
	global_store_dword v[68:69], v58, off offset:64
	v_add_f32_e32 v58, v156, v61
	global_store_dword v[64:65], v58, off offset:64
	v_add_u32_e32 v58, 0x90, v150
	v_mad_i64_i32 v[58:59], s[0:1], v58, s9, 0
	v_add_f32_e32 v54, v155, v54
	v_lshl_add_u64 v[58:59], v[58:59], 2, v[0:1]
	global_store_dword v[58:59], v54, off
	v_add_u32_e32 v54, 0x91, v150
	v_add_f32_e32 v60, v155, v55
	v_mad_i64_i32 v[54:55], s[0:1], v54, s9, 0
	v_lshl_add_u64 v[54:55], v[54:55], 2, v[0:1]
	global_store_dword v[54:55], v60, off
	v_add_u32_e32 v60, 0x92, v150
	v_mad_i64_i32 v[60:61], s[0:1], v60, s9, 0
	v_add_f32_e32 v56, v155, v56
	v_lshl_add_u64 v[60:61], v[60:61], 2, v[0:1]
	global_store_dword v[60:61], v56, off
	v_add_u32_e32 v56, 0x93, v150
	v_add_f32_e32 v70, v155, v57
	v_mad_i64_i32 v[56:57], s[0:1], v56, s9, 0
	v_lshl_add_u64 v[56:57], v[56:57], 2, v[0:1]
	v_add_f32_e32 v50, v156, v50
	global_store_dword v[56:57], v70, off
	global_store_dword v[58:59], v50, off offset:64
	v_add_f32_e32 v50, v156, v51
	global_store_dword v[54:55], v50, off offset:64
	v_add_f32_e32 v50, v156, v52
	global_store_dword v[60:61], v50, off offset:64
	v_add_f32_e32 v50, v156, v53
	global_store_dword v[56:57], v50, off offset:64
	v_add_u32_e32 v50, 0xa0, v150
	v_mad_i64_i32 v[50:51], s[0:1], v50, s9, 0
	v_add_f32_e32 v46, v155, v46
	v_lshl_add_u64 v[50:51], v[50:51], 2, v[0:1]
	global_store_dword v[50:51], v46, off
	v_add_u32_e32 v46, 0xa1, v150
	v_add_f32_e32 v52, v155, v47
	v_mad_i64_i32 v[46:47], s[0:1], v46, s9, 0
	v_lshl_add_u64 v[46:47], v[46:47], 2, v[0:1]
	global_store_dword v[46:47], v52, off
	v_add_u32_e32 v52, 0xa2, v150
	v_mad_i64_i32 v[52:53], s[0:1], v52, s9, 0
	v_add_f32_e32 v48, v155, v48
	v_lshl_add_u64 v[52:53], v[52:53], 2, v[0:1]
	global_store_dword v[52:53], v48, off
	v_add_u32_e32 v48, 0xa3, v150
	v_add_f32_e32 v70, v155, v49
	v_mad_i64_i32 v[48:49], s[0:1], v48, s9, 0
	v_lshl_add_u64 v[48:49], v[48:49], 2, v[0:1]
	v_add_f32_e32 v42, v156, v42
	global_store_dword v[48:49], v70, off
	global_store_dword v[50:51], v42, off offset:64
	v_add_f32_e32 v42, v156, v43
	global_store_dword v[46:47], v42, off offset:64
	v_add_f32_e32 v42, v156, v44
	global_store_dword v[52:53], v42, off offset:64
	v_add_f32_e32 v42, v156, v45
	global_store_dword v[48:49], v42, off offset:64
	v_add_u32_e32 v42, 0xb0, v150
	v_mad_i64_i32 v[42:43], s[0:1], v42, s9, 0
	v_add_f32_e32 v38, v158, v38
	v_lshl_add_u64 v[42:43], v[42:43], 2, v[0:1]
	global_store_dword v[42:43], v38, off
	v_add_u32_e32 v38, 0xb1, v150
	v_add_f32_e32 v44, v158, v39
	v_mad_i64_i32 v[38:39], s[0:1], v38, s9, 0
	v_lshl_add_u64 v[38:39], v[38:39], 2, v[0:1]
	global_store_dword v[38:39], v44, off
	v_add_u32_e32 v44, 0xb2, v150
	v_mad_i64_i32 v[44:45], s[0:1], v44, s9, 0
	v_add_f32_e32 v40, v158, v40
	v_lshl_add_u64 v[44:45], v[44:45], 2, v[0:1]
	global_store_dword v[44:45], v40, off
	v_add_u32_e32 v40, 0xb3, v150
	v_add_f32_e32 v70, v158, v41
	v_mad_i64_i32 v[40:41], s[0:1], v40, s9, 0
	v_lshl_add_u64 v[0:1], v[40:41], 2, v[0:1]
	v_add_f32_e32 v34, v157, v34
	global_store_dword v[0:1], v70, off
	global_store_dword v[42:43], v34, off offset:64
	v_add_f32_e32 v34, v157, v35
	global_store_dword v[38:39], v34, off offset:64
	v_add_f32_e32 v34, v157, v36
	global_store_dword v[44:45], v34, off offset:64
	v_add_f32_e32 v34, v157, v37
	s_waitcnt vmcnt(62)
	v_add_f32_e32 v30, v99, v30
	global_store_dword v[0:1], v34, off offset:64
	global_store_dword v[66:67], v30, off offset:512
	v_add_f32_e32 v30, v99, v31
	global_store_dword v[62:63], v30, off offset:512
	v_add_f32_e32 v30, v99, v32
	global_store_dword v[68:69], v30, off offset:512
	v_add_f32_e32 v30, v99, v33
	v_add_f32_e32 v26, v98, v26
	global_store_dword v[64:65], v30, off offset:512
	global_store_dword v[66:67], v26, off offset:576
	v_add_f32_e32 v26, v98, v27
	global_store_dword v[62:63], v26, off offset:576
	v_add_f32_e32 v26, v98, v28
	global_store_dword v[68:69], v26, off offset:576
	v_add_f32_e32 v26, v98, v29
	v_add_f32_e32 v22, v99, v22
	global_store_dword v[64:65], v26, off offset:576
	global_store_dword v[58:59], v22, off offset:512
	v_add_f32_e32 v22, v99, v23
	global_store_dword v[54:55], v22, off offset:512
	v_add_f32_e32 v22, v99, v24
	global_store_dword v[60:61], v22, off offset:512
	v_add_f32_e32 v22, v99, v25
	v_add_f32_e32 v18, v98, v18
	global_store_dword v[56:57], v22, off offset:512
	global_store_dword v[58:59], v18, off offset:576
	v_add_f32_e32 v18, v98, v19
	global_store_dword v[54:55], v18, off offset:576
	v_add_f32_e32 v18, v98, v20
	global_store_dword v[60:61], v18, off offset:576
	v_add_f32_e32 v18, v98, v21
	v_add_f32_e32 v14, v99, v14
	global_store_dword v[56:57], v18, off offset:576
	global_store_dword v[50:51], v14, off offset:512
	v_add_f32_e32 v14, v99, v15
	global_store_dword v[46:47], v14, off offset:512
	v_add_f32_e32 v14, v99, v16
	global_store_dword v[52:53], v14, off offset:512
	v_add_f32_e32 v14, v99, v17
	v_add_f32_e32 v10, v98, v10
	global_store_dword v[48:49], v14, off offset:512
	global_store_dword v[50:51], v10, off offset:576
	v_add_f32_e32 v10, v98, v11
	global_store_dword v[46:47], v10, off offset:576
	v_add_f32_e32 v10, v98, v12
	global_store_dword v[52:53], v10, off offset:576
	v_add_f32_e32 v10, v98, v13
	v_add_f32_e32 v6, v99, v6
	global_store_dword v[48:49], v10, off offset:576
	global_store_dword v[42:43], v6, off offset:512
	v_add_f32_e32 v6, v99, v7
	global_store_dword v[38:39], v6, off offset:512
	v_add_f32_e32 v6, v99, v8
	global_store_dword v[44:45], v6, off offset:512
	v_add_f32_e32 v6, v99, v9
	v_add_f32_e32 v2, v98, v2
	global_store_dword v[0:1], v6, off offset:512
	global_store_dword v[42:43], v2, off offset:576
	v_add_f32_e32 v2, v98, v3
	global_store_dword v[38:39], v2, off offset:576
	v_add_f32_e32 v2, v98, v4
	global_store_dword v[44:45], v2, off offset:576
	v_add_f32_e32 v2, v98, v5
	global_store_dword v[0:1], v2, off offset:576
	s_endpgm
	s_nop 0
	s_nop 0
	s_nop 0
	s_nop 0
	s_nop 0
	s_nop 0
	s_nop 0
	s_endpgm

.LBB4_11:
	ds_read_b128 v[8:11], v6
	ds_read_b128 v[12:15], v7
	ds_read_b128 v[16:19], v7 offset:16640
	ds_read_b128 v[20:23], v4
	v_add_u32_e32 v28, s4, v0
	v_add_u32_e32 v26, s4, v5
	v_add_u32_e32 v29, s4, v1
	s_add_i32 s4, s4, 64
	v_mad_i64_i32 v[24:25], s[0:1], v28, s16, 0
	v_add_u32_e32 v30, 32, v28
	v_add_u32_e32 v4, 0x8200, v4
	v_add_u32_e32 v6, 0x8200, v6
	v_add_u32_e32 v7, 0x8200, v7
	v_mad_i64_i32 v[26:27], s[0:1], v26, s16, 0
	v_mad_i64_i32 v[28:29], s[0:1], v29, s16, 0
	s_cmpk_eq_i32 s4, 0x100
	v_lshl_add_u64 v[24:25], v[24:25], 1, v[2:3]
	v_mad_i64_i32 v[30:31], s[0:1], v30, s16, 0
	v_lshl_add_u64 v[26:27], v[26:27], 1, v[2:3]
	v_lshl_add_u64 v[28:29], v[28:29], 1, v[2:3]
	v_lshl_add_u64 v[30:31], v[30:31], 1, v[2:3]
	s_waitcnt lgkmcnt(2)
	global_store_dwordx4 v[24:25], v[12:15], off
	global_store_dwordx4 v[26:27], v[8:11], off
	s_waitcnt lgkmcnt(1)
	global_store_dwordx4 v[30:31], v[16:19], off
	s_waitcnt lgkmcnt(0)
	global_store_dwordx4 v[28:29], v[20:23], off
	s_cbranch_scc0 .LBB4_11
	s_endpgm
	s_nop 0
	s_nop 0
	s_nop 0
	s_nop 0
	s_nop 0
	s_nop 0
	s_nop 0
	s_nop 0
	s_nop 0
	s_nop 0
	s_nop 0
	s_nop 0
	s_nop 0
	s_nop 0
	s_nop 0
	s_nop 0
	s_nop 0
	s_nop 0
	s_nop 0
	s_nop 0
	s_nop 0
	s_nop 0
	s_nop 0
	s_nop 0
	s_nop 0
	s_nop 0
	s_nop 0
	s_nop 0
	s_nop 0
	s_nop 0
	s_nop 0
	s_nop 0
	s_nop 0
	s_nop 0
	s_nop 0
	s_nop 0
	s_endpgm
